# split-K exchange in phase 1: L1 invalidate dropped (the peer partial is read with sc1 loads that bypass L1; partner workgroups share the XCD)
# baseline (speedup 1.0000x reference)
;     ...
;                 if (wid == 0) { if (lane == 0) { unsigned sp = 0; while (__hip_atomic_load(fwait, RLX_AGENT) < ks_epoch) { __builtin_amdgcn_s_sleep(2); if (++sp > (1u << 20)) break; } }
;                     __builtin_amdgcn_fence(__ATOMIC_ACQUIRE, "agent"); asm volatile("s_waitcnt vmcnt(0)" ::: "memory"); }
;                 asm volatile("" ::: "memory"); __builtin_amdgcn_s_barrier(); asm volatile("" ::: "memory");
.LBB0_566:
	s_or_b64 exec, exec, s[86:87]
	s_waitcnt vmcnt(0)
	s_waitcnt vmcnt(0)
